# tail-aware stagger with 1.7us steps (s_sleep 64), index wg>>5
# baseline (speedup 1.0000x reference)
.Lstg_loop:
	s_sleep 64
	s_add_i32 s98, s98, -1
	s_cmp_lg_u32 s98, 0
	s_cbranch_scc1 .Lstg_loop
